# gqa16 tile loop: the last 4 bf16 packs of P moved from in front of the barrier into the K-read latency gap behind it
# baseline (speedup 1.0000x reference)
; #define SBAR() __builtin_amdgcn_sched_barrier(0)
; template <int LDQ, int LDK, int LDO>
; __device__ __forceinline__ void attn_gqa16_body(const bf16* __restrict__ Qb, const bf16* __restrict__ Kh, const bf16* __restrict__ Vh, bf16* __restrict__ Ob, int seq, char* lds, float mref) {
;     ...
;     HPACK();
;     __syncthreads();
;     const bool more = t + 1 < NT;
;     if (more) HQK((t + 1) & 1);
;     const int vb = vb0 + (t & 1) * (int)G16_V;
;     SBAR(); pv16<0>(o, vb, pb); SBAR();
.LBB0_650:
	s_add_i32 s17, s16, 1
	s_and_b32 s16, s16, 1
	s_and_b32 s46, 1, s17
	s_cmp_eq_u32 s46, 1
	s_cselect_b32 s85, s86, s84
	s_cselect_b32 s46, 0x4400, 0
	v_add_u32_e32 v189, s46, v182
	s_waitcnt vmcnt(2)
	s_barrier
	ds_read_b128 v[130:133], v189 offset:33280
	ds_read_b128 v[146:149], v189 offset:33344
	ds_read_b128 v[200:203], v189 offset:37632
	ds_read_b128 v[204:207], v189 offset:37696
	ds_read_b128 v[212:215], v189 offset:41984
	ds_read_b128 v[216:219], v189 offset:42048
	ds_read_b128 v[224:227], v189 offset:46336
	ds_read_b128 v[228:231], v189 offset:46400
	s_mov_b32 m0, s85
	s_nop 0
	global_load_lds_dwordx4 v253, s[74:75]
	s_add_i32 m0, s85, 0x400
	s_nop 0
	global_load_lds_dwordx4 v253, s[76:77]
	s_add_u32 s74, s74, 0x90000
	s_addc_u32 s75, s75, 0
	s_add_u32 s76, s76, 0x90000
	s_addc_u32 s77, s77, 0
	v_cvt_pk_bf16_f32 v124, v134, v138
	v_cvt_pk_bf16_f32 v125, v136, v140
	v_cvt_pk_bf16_f32 v128, v135, v139
	v_cvt_pk_bf16_f32 v129, v137, v141
	s_waitcnt lgkmcnt(7)
	v_mfma_f32_16x16x32_bf16 v[196:199], v[130:133], v[30:33], v[248:251]
	v_add_f32_e64 v134, v134, v138
	v_add_f32_e64 v135, v135, v139
	v_pk_add_f32 v[136:137], v[136:137], v[140:141]
	s_mul_i32 s46, s16, 0x4100
	v_mfma_f32_16x16x32_bf16 v[130:133], v[130:133], v[38:41], v[248:251]
	v_cvt_pk_bf16_f32 v114, v246, v152
	s_waitcnt lgkmcnt(5)
	v_mfma_f32_16x16x32_bf16 v[208:211], v[200:203], v[30:33], v[248:251]
	v_cvt_pk_bf16_f32 v115, v240, v160
	v_mfma_f32_16x16x32_bf16 v[200:203], v[200:203], v[38:41], v[248:251]
	v_cvt_pk_bf16_f32 v116, v168, v170
	s_waitcnt lgkmcnt(3)
	v_mfma_f32_16x16x32_bf16 v[220:223], v[212:215], v[30:33], v[248:251]
	v_cvt_pk_bf16_f32 v117, v242, v244
	v_mfma_f32_16x16x32_bf16 v[212:215], v[212:215], v[38:41], v[248:251]
	v_cvt_pk_bf16_f32 v118, v247, v153
	s_waitcnt lgkmcnt(1)
	v_mfma_f32_16x16x32_bf16 v[232:235], v[224:227], v[30:33], v[248:251]
	v_cvt_pk_bf16_f32 v119, v241, v161
	v_mfma_f32_16x16x32_bf16 v[224:227], v[224:227], v[38:41], v[248:251]
	v_cvt_pk_bf16_f32 v120, v169, v171
	v_mfma_f32_16x16x32_bf16 v[196:199], v[146:149], v[18:21], v[196:199]
	v_cvt_pk_bf16_f32 v121, v243, v245
	v_mfma_f32_16x16x32_bf16 v[130:133], v[146:149], v[22:25], v[130:133]
	v_cvt_pk_bf16_f32 v122, v142, v172
	v_mfma_f32_16x16x32_bf16 v[146:149], v[204:207], v[18:21], v[208:211]
	v_cvt_pk_bf16_f32 v123, v144, v174
	v_mfma_f32_16x16x32_bf16 v[200:203], v[204:207], v[22:25], v[200:203]
	v_cvt_pk_bf16_f32 v126, v143, v173
	v_mfma_f32_16x16x32_bf16 v[204:207], v[216:219], v[18:21], v[220:223]
	v_cvt_pk_bf16_f32 v127, v145, v175
	v_mfma_f32_16x16x32_bf16 v[208:211], v[216:219], v[22:25], v[212:215]
	s_waitcnt lgkmcnt(0)
	v_mfma_f32_16x16x32_bf16 v[216:219], v[228:231], v[22:25], v[224:227]
	ds_read_b128 v[220:223], v189 offset:33408
	s_nop 1
	ds_read_b128 v[224:227], v189 offset:33472
	v_mfma_f32_16x16x32_bf16 v[212:215], v[228:231], v[18:21], v[232:235]
	s_waitcnt lgkmcnt(1)
	v_mfma_f32_16x16x32_bf16 v[196:199], v[220:223], v[10:13], v[196:199]
	v_mfma_f32_16x16x32_bf16 v[130:133], v[220:223], v[14:17], v[130:133]
	ds_read_b128 v[220:223], v189 offset:37760
	ds_read_b128 v[228:231], v189 offset:37824
	s_waitcnt lgkmcnt(1)
	v_mfma_f32_16x16x32_bf16 v[146:149], v[220:223], v[10:13], v[146:149]
	v_mfma_f32_16x16x32_bf16 v[200:203], v[220:223], v[14:17], v[200:203]
	ds_read_b128 v[220:223], v189 offset:42112
	ds_read_b128 v[232:235], v189 offset:42176
	s_waitcnt lgkmcnt(1)
	v_mfma_f32_16x16x32_bf16 v[204:207], v[220:223], v[10:13], v[204:207]
	v_mfma_f32_16x16x32_bf16 v[208:211], v[220:223], v[14:17], v[208:211]
	ds_read_b128 v[220:223], v189 offset:46464
	ds_read_b128 v[236:239], v189 offset:46528
	v_add_u32_e32 v189, s46, v183
	s_waitcnt lgkmcnt(1)
	v_mfma_f32_16x16x32_bf16 v[212:215], v[220:223], v[10:13], v[212:215]
	v_mfma_f32_16x16x32_bf16 v[216:219], v[220:223], v[14:17], v[216:219]
	v_mfma_f32_16x16x32_bf16 v[220:223], v[224:227], v[6:9], v[130:133]
	s_nop 2
	v_add_f32_e64 v130, v246, v152
	v_add_f32_e64 v131, v247, v153
	v_pk_add_f32 v[132:133], v[240:241], v[160:161]
	v_pk_add_f32 v[152:153], v[168:169], v[170:171]
	v_pk_add_f32 v[156:157], v[242:243], v[244:245]
	v_pk_add_f32 v[158:159], v[142:143], v[172:173]
	v_pk_add_f32 v[160:161], v[144:145], v[174:175]
	v_pk_add_f32 v[130:131], v[130:131], v[132:133]
	v_mfma_f32_16x16x32_bf16 v[142:145], v[232:235], v[2:5], v[204:207]
	v_add_f32_e64 v152, v152, v156
	v_add_f32_e64 v153, v153, v157
	v_pk_add_f32 v[156:157], v[158:159], v[160:161]
	v_pk_add_f32 v[158:159], v[134:135], v[136:137]
	v_mfma_f32_16x16x32_bf16 v[138:141], v[232:235], v[6:9], v[208:211]
	v_add_f32_e64 v150, v150, v130
	v_add_f32_e64 v151, v151, v131
	v_pk_add_f32 v[150:151], v[152:153], v[150:151]
	s_waitcnt lgkmcnt(0)
	v_mfma_f32_16x16x32_bf16 v[134:137], v[236:239], v[2:5], v[212:215]
	v_add_f32_e64 v150, v156, v150
	v_add_f32_e64 v151, v157, v151
	v_pk_add_f32 v[150:151], v[158:159], v[150:151]
	v_mfma_f32_16x16x32_bf16 v[196:199], v[224:227], v[2:5], v[196:199]
	v_mfma_f32_16x16x32_bf16 v[224:227], v[228:231], v[2:5], v[146:149]
	v_mfma_f32_16x16x32_bf16 v[146:149], v[228:231], v[6:9], v[200:203]
	v_mfma_f32_16x16x32_bf16 v[130:133], v[236:239], v[6:9], v[216:219]
	ds_read_b64_tr_b16 v[156:157], v189 offset:0
	ds_read_b64_tr_b16 v[158:159], v189 offset:0x200
	ds_read_b64_tr_b16 v[164:165], v189 offset:0x400
	ds_read_b64_tr_b16 v[166:167], v189 offset:0x600
	ds_read_b64_tr_b16 v[168:169], v189 offset:0x820
	ds_read_b64_tr_b16 v[170:171], v189 offset:0xa20
	ds_read_b64_tr_b16 v[172:173], v189 offset:0xc20
	ds_read_b64_tr_b16 v[174:175], v189 offset:0xe20
	ds_read_b64_tr_b16 v[200:201], v189 offset:0x1040
	ds_read_b64_tr_b16 v[202:203], v189 offset:0x1240
	ds_read_b64_tr_b16 v[204:205], v189 offset:0x1440
	ds_read_b64_tr_b16 v[206:207], v189 offset:0x1640
	s_waitcnt lgkmcnt(4)
; template <int D0> __device__ __forceinline__ void pv16(f32x4a (&o)[8][2], int vb, const bf16x8 (&pb)[2][2]) {
;     ...
;   const s16x4 a0 = TR(D0, 0, 0), a1 = TR(D0, 0, 1), a2 = TR(D0, 1, 0), a3 = TR(D0, 1, 1), b0 = TR(D0 + 1, 0, 0), b1 = TR(D0 + 1, 0, 1), b2 = TR(D0 + 1, 1, 0), b3 = TR(D0 + 1, 1, 1);
;   const s16x4 c0 = TR(D0 + 2, 0, 0), c1 = TR(D0 + 2, 0, 1), c2 = TR(D0 + 2, 1, 0), c3 = TR(D0 + 2, 1, 1);
;   asm volatile("s_waitcnt lgkmcnt(4)" ::: "memory"); SBAR();
;   o[D0][0] = MFMA16(PK16(a0, a1), pb[0][0], o[D0][0]); o[D0][1] = MFMA16(PK16(a0, a1), pb[0][1], o[D0][1]);
;   o[D0 + 1][0] = MFMA16(PK16(b0, b1), pb[0][0], o[D0 + 1][0]); o[D0 + 1][1] = MFMA16(PK16(b0, b1), pb[0][1], o[D0 + 1][1]);
;   o[D0][0] = MFMA16(PK16(a2, a3), pb[1][0], o[D0][0]); o[D0][1] = MFMA16(PK16(a2, a3), pb[1][1], o[D0][1]);
;   o[D0 + 1][0] = MFMA16(PK16(b2, b3), pb[1][0], o[D0 + 1][0]); o[D0 + 1][1] = MFMA16(PK16(b2, b3), pb[1][1], o[D0 + 1][1]);
;   SBAR();
;   const s16x4 d0 = TR(D0 + 3, 0, 0), d1 = TR(D0 + 3, 0, 1), d2 = TR(D0 + 3, 1, 0), d3 = TR(D0 + 3, 1, 1);
;   asm volatile("s_waitcnt lgkmcnt(4)" ::: "memory"); SBAR();
;   o[D0 + 2][0] = MFMA16(PK16(c0, c1), pb[0][0], o[D0 + 2][0]); o[D0 + 2][1] = MFMA16(PK16(c0, c1), pb[0][1], o[D0 + 2][1]);
;   o[D0 + 2][0] = MFMA16(PK16(c2, c3), pb[1][0], o[D0 + 2][0]); o[D0 + 2][1] = MFMA16(PK16(c2, c3), pb[1][1], o[D0 + 2][1]);
;   asm volatile("s_waitcnt lgkmcnt(0)" ::: "memory"); SBAR();
;   o[D0 + 3][0] = MFMA16(PK16(d0, d1), pb[0][0], o[D0 + 3][0]); o[D0 + 3][1] = MFMA16(PK16(d0, d1), pb[0][1], o[D0 + 3][1]);
;   o[D0 + 3][0] = MFMA16(PK16(d2, d3), pb[1][0], o[D0 + 3][0]); o[D0 + 3][1] = MFMA16(PK16(d2, d3), pb[1][1], o[D0 + 3][1]);
; template <int LDQ, int LDK, int LDO>
; __device__ __forceinline__ void attn_gqa16_body(const bf16* __restrict__ Qb, const bf16* __restrict__ Kh, const bf16* __restrict__ Vh, bf16* __restrict__ Ob, int seq, char* lds, float mref) {
;     ...
;     HPACK();
;     __syncthreads();
;     const bool more = t + 1 < NT;
;     if (more) HQK((t + 1) & 1);
;     const int vb = vb0 + (t & 1) * (int)G16_V;
;     SBAR(); pv16<0>(o, vb, pb); SBAR();
;     asm volatile("s_waitcnt vmcnt(0)" ::: "memory");
;     if (t + 2 < NT) HWRITEK(t & 1);
;     if (t + 1 < NT) HWRITEV((t + 1) & 1);
;     HLOADK(t + 3); HLOADV(t + 2);
;     SBAR(); pv16<4>(o, vb, pb); SBAR();
;     if (more) HEXP();
	s_nop 0
	v_mfma_f32_16x16x32_bf16 v[102:105], v[156:159], v[114:117], v[102:105]
	v_mfma_f32_16x16x32_bf16 v[98:101], v[156:159], v[118:121], v[98:101]
	v_mfma_f32_16x16x32_bf16 v[94:97], v[168:171], v[114:117], v[94:97]
	v_exp_f32_e32 v246, v196
	v_mfma_f32_16x16x32_bf16 v[90:93], v[168:171], v[118:121], v[90:93]
	v_exp_f32_e32 v240, v198
	v_mfma_f32_16x16x32_bf16 v[102:105], v[164:167], v[122:125], v[102:105]
	v_exp_f32_e32 v160, v199
	v_mfma_f32_16x16x32_bf16 v[98:101], v[164:167], v[126:129], v[98:101]
	v_exp_f32_e32 v247, v220
	v_mfma_f32_16x16x32_bf16 v[94:97], v[172:175], v[122:125], v[94:97]
	v_exp_f32_e32 v241, v222
	v_mfma_f32_16x16x32_bf16 v[90:93], v[172:175], v[126:129], v[90:93]
	v_exp_f32_e32 v161, v223
	ds_read_b64_tr_b16 v[156:157], v189 offset:0x1860
	ds_read_b64_tr_b16 v[158:159], v189 offset:0x1a60
	ds_read_b64_tr_b16 v[164:165], v189 offset:0x1c60
	ds_read_b64_tr_b16 v[166:167], v189 offset:0x1e60
	s_waitcnt lgkmcnt(4)
	v_mfma_f32_16x16x32_bf16 v[78:81], v[200:203], v[114:117], v[78:81]
	v_exp_f32_e32 v242, v226
	s_waitcnt lgkmcnt(0)
	v_mfma_f32_16x16x32_bf16 v[50:53], v[200:203], v[118:121], v[50:53]
	v_exp_f32_e32 v244, v227
	v_mfma_f32_16x16x32_bf16 v[78:81], v[204:207], v[122:125], v[78:81]
	v_exp_f32_e32 v243, v148
	v_mfma_f32_16x16x32_bf16 v[50:53], v[204:207], v[126:129], v[50:53]
	v_exp_f32_e32 v245, v149
	v_mfma_f32_16x16x32_bf16 v[82:85], v[156:159], v[114:117], v[82:85]
	v_exp_f32_e32 v142, v142
	v_mfma_f32_16x16x32_bf16 v[86:89], v[156:159], v[118:121], v[86:89]
	v_exp_f32_e32 v144, v144
	v_mfma_f32_16x16x32_bf16 v[82:85], v[164:167], v[122:125], v[82:85]
	v_exp_f32_e32 v134, v134
	v_mfma_f32_16x16x32_bf16 v[86:89], v[164:167], v[126:129], v[86:89]
	v_exp_f32_e32 v136, v136
	v_lshl_add_u64 v[152:153], v[162:163], 0, s[14:15]
	v_add_co_u32_e32 v156, vcc, s37, v152
	s_mulk_i32 s16, 0x4400
	s_nop 0
	v_addc_co_u32_e32 v157, vcc, 0, v153, vcc
	v_add_co_u32_e32 v158, vcc, s38, v152
	v_add_u32_e32 v164, s16, v194
	s_nop 0
	v_addc_co_u32_e32 v159, vcc, 0, v153, vcc
	s_waitcnt vmcnt(2)
	ds_write_b128 v164, v[106:109] offset:33280
	ds_write_b128 v164, v[110:113] offset:41984
	global_load_dwordx4 v[106:109], v[156:157], off offset:3072
	global_load_dwordx4 v[110:113], v[158:159], off offset:3072
	ds_read_b64_tr_b16 v[156:157], v189 offset:0x2080
	ds_read_b64_tr_b16 v[158:159], v189 offset:0x2280
	ds_read_b64_tr_b16 v[164:165], v189 offset:0x2480
	ds_read_b64_tr_b16 v[166:167], v189 offset:0x2680
	ds_read_b64_tr_b16 v[168:169], v189 offset:0x28a0
	ds_read_b64_tr_b16 v[170:171], v189 offset:0x2aa0
	ds_read_b64_tr_b16 v[172:173], v189 offset:0x2ca0
	ds_read_b64_tr_b16 v[174:175], v189 offset:0x2ea0
	ds_read_b64_tr_b16 v[200:201], v189 offset:0x30c0
	ds_read_b64_tr_b16 v[202:203], v189 offset:0x32c0
	ds_read_b64_tr_b16 v[204:205], v189 offset:0x34c0
	ds_read_b64_tr_b16 v[206:207], v189 offset:0x36c0
	s_waitcnt lgkmcnt(4)
	s_nop 0
	v_mfma_f32_16x16x32_bf16 v[54:57], v[156:159], v[114:117], v[54:57]
	v_exp_f32_e32 v152, v197
	v_mfma_f32_16x16x32_bf16 v[62:65], v[156:159], v[118:121], v[62:65]
	v_exp_f32_e32 v153, v221
	v_mfma_f32_16x16x32_bf16 v[58:61], v[168:171], v[114:117], v[58:61]
	v_mfma_f32_16x16x32_bf16 v[70:73], v[168:171], v[118:121], v[70:73]
	v_mfma_f32_16x16x32_bf16 v[54:57], v[164:167], v[122:125], v[54:57]
	v_mfma_f32_16x16x32_bf16 v[62:65], v[164:167], v[126:129], v[62:65]
	v_mfma_f32_16x16x32_bf16 v[58:61], v[172:175], v[122:125], v[58:61]
	v_mfma_f32_16x16x32_bf16 v[70:73], v[172:175], v[126:129], v[70:73]
	ds_read_b64_tr_b16 v[156:157], v189 offset:0x38e0
	ds_read_b64_tr_b16 v[158:159], v189 offset:0x3ae0
	ds_read_b64_tr_b16 v[164:165], v189 offset:0x3ce0
	ds_read_b64_tr_b16 v[166:167], v189 offset:0x3ee0
	s_waitcnt lgkmcnt(4)
	v_mfma_f32_16x16x32_bf16 v[42:45], v[200:203], v[114:117], v[42:45]
	v_exp_f32_e32 v168, v224
	v_exp_f32_e32 v170, v225
	s_waitcnt lgkmcnt(0)
	v_mfma_f32_16x16x32_bf16 v[46:49], v[200:203], v[118:121], v[46:49]
	v_exp_f32_e32 v169, v146
	v_exp_f32_e32 v171, v147
	v_mfma_f32_16x16x32_bf16 v[42:45], v[204:207], v[122:125], v[42:45]
	v_exp_f32_e32 v172, v143
	v_exp_f32_e32 v174, v145
	v_mfma_f32_16x16x32_bf16 v[46:49], v[204:207], v[126:129], v[46:49]
	v_exp_f32_e32 v143, v138
	v_exp_f32_e32 v173, v139
	v_mfma_f32_16x16x32_bf16 v[66:69], v[156:159], v[114:117], v[66:69]
	v_exp_f32_e32 v145, v140
	v_exp_f32_e32 v175, v141
	v_mfma_f32_16x16x32_bf16 v[74:77], v[156:159], v[118:121], v[74:77]
	v_exp_f32_e32 v138, v135
	v_exp_f32_e32 v140, v137
	v_mfma_f32_16x16x32_bf16 v[66:69], v[164:167], v[122:125], v[66:69]
	v_exp_f32_e32 v135, v130
	v_exp_f32_e32 v139, v131
	v_mfma_f32_16x16x32_bf16 v[74:77], v[164:167], v[126:129], v[74:77]
	v_exp_f32_e32 v137, v132
	v_exp_f32_e32 v141, v133
	s_add_u32 s14, s14, 0x90000
	s_addc_u32 s15, s15, 0
	s_cmp_lg_u32 s14, 0x9120000
	s_mov_b32 s16, s17
	s_cbranch_scc1 .LBB0_650
	v_mov_b32_e32 v156, v240
	v_mov_b32_e32 v157, v241
	v_mov_b32_e32 v158, v246
	v_mov_b32_e32 v159, v247
	v_mov_b32_e32 v164, v242
	v_mov_b32_e32 v165, v243
	v_mov_b32_e32 v166, v244
	v_mov_b32_e32 v167, v245
	s_waitcnt vmcnt(1)
	v_cvt_pk_bf16_f32 v106, v158, v152
	v_cvt_pk_bf16_f32 v107, v156, v160
	v_cvt_pk_bf16_f32 v108, v168, v170
	v_cvt_pk_bf16_f32 v109, v164, v166
	s_waitcnt vmcnt(0)
	v_cvt_pk_bf16_f32 v110, v159, v153
	v_cvt_pk_bf16_f32 v111, v157, v161
	v_cvt_pk_bf16_f32 v112, v169, v171
	v_cvt_pk_bf16_f32 v113, v165, v167
	v_cvt_pk_bf16_f32 v114, v142, v172
	v_cvt_pk_bf16_f32 v115, v144, v174
	v_cvt_pk_bf16_f32 v116, v134, v138
	v_cvt_pk_bf16_f32 v117, v136, v140
	v_cvt_pk_bf16_f32 v118, v143, v173
	v_cvt_pk_bf16_f32 v119, v145, v175
	v_cvt_pk_bf16_f32 v120, v135, v139
	v_cvt_pk_bf16_f32 v121, v137, v141
	s_waitcnt lgkmcnt(0)
	s_barrier
; #define SBAR() __builtin_amdgcn_sched_barrier(0)
; #define HLOADV(kt) do { const char* vb_ = (const char*)Vh + (size_t)(kt) * (64 * LDK * 2); sv0 = *(const bf16x8*)(vb_ + koff0); sv1 = *(const bf16x8*)(vb_ + koff1); } while (0)
; #define HLOADK(kt) do { const char* kb_ = (const char*)Kh + (size_t)(kt) * (64 * LDK * 2); sk0 = *(const bf16x8*)(kb_ + koff0); sk1 = *(const bf16x8*)(kb_ + koff1); } while (0)
; #define HWRITEV(b) do { char* d_ = V_lds + (b) * G16_V; *(bf16x8*)(d_ + vst0) = sv0; *(bf16x8*)(d_ + vst1) = sv1; } while (0)
; #define HWRITEK(b) do { char* d_ = K_lds + (b) * GB_K; *(bf16x8*)(d_ + KSWZ(sr, sc * 2)) = sk0; *(bf16x8*)(d_ + KSWZ(32 + sr, sc * 2)) = sk1; } while (0)
; template <int LDQ, int LDK, int LDO>
; __device__ __forceinline__ void attn_gqa16_body(const bf16* __restrict__ Qb, const bf16* __restrict__ Kh, const bf16* __restrict__ Vh, bf16* __restrict__ Ob, int seq, char* lds, float mref) {
;     ...
;     HPACK();
;     __syncthreads();
;     const bool more = t + 1 < NT;
;     if (more) HQK((t + 1) & 1);
;     const int vb = vb0 + (t & 1) * (int)G16_V;
;     SBAR(); pv16<0>(o, vb, pb); SBAR();
;     asm volatile("s_waitcnt vmcnt(0)" ::: "memory");
;     if (t + 2 < NT) HWRITEK(t & 1);
;     if (t + 1 < NT) HWRITEV((t + 1) & 1);
;     HLOADK(t + 3); HLOADV(t + 2);
;     SBAR(); pv16<4>(o, vb, pb); SBAR();
	s_mov_b32 m0, s86
	s_nop 0
	global_load_lds_dwordx4 v253, s[74:75]
	s_add_i32 m0, s86, 0x400
	s_nop 0
	global_load_lds_dwordx4 v253, s[76:77]
	ds_read_b128 v[122:125], v182 offset:50688
	ds_read_b128 v[126:129], v182 offset:50752
	ds_read_b128 v[146:149], v182 offset:55040
	ds_read_b128 v[196:199], v182 offset:55104
	ds_read_b128 v[204:207], v182 offset:59392
	ds_read_b128 v[208:211], v182 offset:59456
	ds_read_b128 v[216:219], v182 offset:63744
	ds_read_b128 v[220:223], v182 offset:63808
	s_waitcnt lgkmcnt(7)
	v_mfma_f32_16x16x32_bf16 v[130:133], v[122:125], v[30:33], 0
	v_mov_b32_e32 v190, v168
	v_mov_b32_e32 v191, v158
	v_mov_b32_e32 v192, v170
	v_mfma_f32_16x16x32_bf16 v[122:125], v[122:125], v[38:41], 0
	v_mov_b32_e32 v193, v152
	v_mov_b32_e32 v152, v171
	s_lshl_b32 s8, s8, 12
	s_waitcnt lgkmcnt(5)
	v_mfma_f32_16x16x32_bf16 v[200:203], v[146:149], v[30:33], 0
	s_add_u32 s8, s42, s8
	s_addc_u32 s14, s43, 0
	s_add_u32 s12, s8, s12
	v_mfma_f32_16x16x32_bf16 v[146:149], v[146:149], v[38:41], 0
	s_addc_u32 s13, s14, s13
	s_waitcnt lgkmcnt(3)
	v_mfma_f32_16x16x32_bf16 v[212:215], v[204:207], v[30:33], 0
	s_waitcnt lgkmcnt(1)
	v_mfma_f32_16x16x32_bf16 v[30:33], v[216:219], v[30:33], 0
	v_mfma_f32_16x16x32_bf16 v[130:133], v[126:129], v[18:21], v[130:133]
	v_mfma_f32_16x16x32_bf16 v[122:125], v[126:129], v[22:25], v[122:125]
	v_mfma_f32_16x16x32_bf16 v[126:129], v[196:199], v[18:21], v[200:203]
	v_mfma_f32_16x16x32_bf16 v[146:149], v[196:199], v[22:25], v[146:149]
	v_mfma_f32_16x16x32_bf16 v[196:199], v[208:211], v[18:21], v[212:215]
	s_waitcnt lgkmcnt(0)
	v_mfma_f32_16x16x32_bf16 v[18:21], v[220:223], v[18:21], v[30:33]
	s_nop 0
	v_mov_b32_e32 v213, v156
	v_mov_b32_e32 v212, v164
	v_mov_b32_e32 v214, v166
	ds_read_b128 v[30:33], v182 offset:50816
	v_mfma_f32_16x16x32_bf16 v[204:207], v[204:207], v[38:41], 0
	v_mov_b32_e32 v215, v160
	v_mfma_f32_16x16x32_bf16 v[38:41], v[216:219], v[38:41], 0
	v_mov_b32_e32 v216, v169
	v_mov_b32_e32 v217, v159
	v_mov_b32_e32 v219, v157
	v_mfma_f32_16x16x32_bf16 v[200:203], v[208:211], v[22:25], v[204:207]
	v_mov_b32_e32 v218, v165
	v_mfma_f32_16x16x32_bf16 v[22:25], v[220:223], v[22:25], v[38:41]
	s_nop 2
	ds_read_b128 v[38:41], v182 offset:55168
	ds_read_b128 v[204:207], v182 offset:50880
	s_waitcnt lgkmcnt(2)
	v_mfma_f32_16x16x32_bf16 v[130:133], v[30:33], v[10:13], v[130:133]
	v_mfma_f32_16x16x32_bf16 v[30:33], v[30:33], v[14:17], v[122:125]
	s_nop 2
	ds_read_b128 v[122:125], v182 offset:59520
	ds_read_b128 v[208:211], v182 offset:55232
	s_waitcnt lgkmcnt(3)
	v_mfma_f32_16x16x32_bf16 v[126:129], v[38:41], v[10:13], v[126:129]
	v_mfma_f32_16x16x32_bf16 v[38:41], v[38:41], v[14:17], v[146:149]
	s_nop 2
	ds_read_b128 v[146:149], v182 offset:63872
	ds_read_b128 v[168:171], v182 offset:59584
	ds_read_b128 v[156:159], v182 offset:63936
	s_waitcnt lgkmcnt(4)
	v_mfma_f32_16x16x32_bf16 v[196:199], v[122:125], v[10:13], v[196:199]
	s_waitcnt lgkmcnt(2)
	v_mfma_f32_16x16x32_bf16 v[10:13], v[146:149], v[10:13], v[18:21]
	v_mfma_f32_16x16x32_bf16 v[122:125], v[122:125], v[14:17], v[200:203]
	s_nop 1
	v_mov_b32_e32 v18, v142
	v_mov_b32_e32 v19, v144
	v_mov_b32_e32 v20, v172
	v_mfma_f32_16x16x32_bf16 v[14:17], v[146:149], v[14:17], v[22:25]
	v_mov_b32_e32 v201, v161
	v_mov_b32_e32 v200, v167
	v_mov_b32_e32 v21, v174
	v_mfma_f32_16x16x32_bf16 v[160:163], v[204:207], v[6:9], v[30:33]
	v_add_f32_e64 v24, v190, v192
	v_add_f32_e64 v25, v191, v193
	v_mov_b32_e32 v144, v143
	v_mov_b32_e32 v22, v173
	v_pk_add_f32 v[30:31], v[212:213], v[214:215]
	v_mfma_f32_16x16x32_bf16 v[146:149], v[204:207], v[2:5], v[130:133]
	v_add_f32_e64 v24, v24, v30
	v_add_f32_e64 v25, v25, v31
	v_mov_b32_e32 v23, v175
	v_pk_add_f32 v[32:33], v[216:217], v[152:153]
	v_mfma_f32_16x16x32_bf16 v[164:167], v[208:211], v[2:5], v[126:129]
	v_add_f32_e64 v144, v144, v22
	v_add_f32_e64 v145, v145, v23
	v_add_f32_e32 v130, v134, v138
	v_add_f32_e32 v132, v136, v140
	v_mfma_f32_16x16x32_bf16 v[172:175], v[208:211], v[6:9], v[38:41]
	v_add_f32_e64 v126, v18, v20
	v_add_f32_e64 v127, v19, v21
	s_nop 0
	v_pk_add_f32 v[38:39], v[218:219], v[200:201]
	s_waitcnt lgkmcnt(1)
	v_mfma_f32_16x16x32_bf16 v[196:199], v[168:171], v[2:5], v[196:199]
	v_add_f32_e64 v142, v32, v38
	v_add_f32_e64 v143, v33, v39
	s_waitcnt lgkmcnt(0)
	v_mfma_f32_16x16x32_bf16 v[200:203], v[156:159], v[2:5], v[10:13]
	v_add_f32_e64 v2, v150, v25
	v_add_f32_e64 v3, v151, v24
	v_pk_add_f32 v[128:129], v[24:25], v[2:3]
	v_mfma_f32_16x16x32_bf16 v[168:171], v[168:171], v[6:9], v[122:125]
	s_nop 2
	v_add_f32_e32 v122, v135, v139
	v_add_f32_e32 v124, v137, v141
	v_mfma_f32_16x16x32_bf16 v[134:137], v[156:159], v[6:9], v[14:17]
	ds_read_b64_tr_b16 v[2:3], v183 offset:0
	ds_read_b64_tr_b16 v[4:5], v183 offset:0x200
	ds_read_b64_tr_b16 v[6:7], v183 offset:0x400
	ds_read_b64_tr_b16 v[8:9], v183 offset:0x600
	ds_read_b64_tr_b16 v[10:11], v183 offset:0x820
	ds_read_b64_tr_b16 v[12:13], v183 offset:0xa20
	ds_read_b64_tr_b16 v[14:15], v183 offset:0xc20
	ds_read_b64_tr_b16 v[16:17], v183 offset:0xe20
	ds_read_b64_tr_b16 v[18:19], v183 offset:0x1040
	ds_read_b64_tr_b16 v[20:21], v183 offset:0x1240
	ds_read_b64_tr_b16 v[22:23], v183 offset:0x1440
	ds_read_b64_tr_b16 v[24:25], v183 offset:0x1640
	s_waitcnt lgkmcnt(4)
	s_nop 0
	v_mfma_f32_16x16x32_bf16 v[30:33], v[2:5], v[106:109], v[102:105]
	v_mfma_f32_16x16x32_bf16 v[38:41], v[2:5], v[110:113], v[98:101]
	v_mfma_f32_16x16x32_bf16 v[94:97], v[10:13], v[106:109], v[94:97]
	v_mfma_f32_16x16x32_bf16 v[10:13], v[10:13], v[110:113], v[90:93]
	v_mfma_f32_16x16x32_bf16 v[2:5], v[6:9], v[114:117], v[30:33]
	v_mfma_f32_16x16x32_bf16 v[6:9], v[6:9], v[118:121], v[38:41]
	v_mfma_f32_16x16x32_bf16 v[38:41], v[14:17], v[114:117], v[94:97]
	v_mfma_f32_16x16x32_bf16 v[90:93], v[14:17], v[118:121], v[10:13]
	ds_read_b64_tr_b16 v[14:15], v183 offset:0x1860
	ds_read_b64_tr_b16 v[16:17], v183 offset:0x1a60
	ds_read_b64_tr_b16 v[30:31], v183 offset:0x1c60
	ds_read_b64_tr_b16 v[32:33], v183 offset:0x1e60
	s_waitcnt lgkmcnt(4)
; #define SBAR() __builtin_amdgcn_sched_barrier(0)
; #define HLOADV(kt) do { const char* vb_ = (const char*)Vh + (size_t)(kt) * (64 * LDK * 2); sv0 = *(const bf16x8*)(vb_ + koff0); sv1 = *(const bf16x8*)(vb_ + koff1); } while (0)
; #define HLOADK(kt) do { const char* kb_ = (const char*)Kh + (size_t)(kt) * (64 * LDK * 2); sk0 = *(const bf16x8*)(kb_ + koff0); sk1 = *(const bf16x8*)(kb_ + koff1); } while (0)
; #define HWRITEV(b) do { char* d_ = V_lds + (b) * G16_V; *(bf16x8*)(d_ + vst0) = sv0; *(bf16x8*)(d_ + vst1) = sv1; } while (0)
; #define HWRITEK(b) do { char* d_ = K_lds + (b) * GB_K; *(bf16x8*)(d_ + KSWZ(sr, sc * 2)) = sk0; *(bf16x8*)(d_ + KSWZ(32 + sr, sc * 2)) = sk1; } while (0)
; #define HEXP() do { _Pragma("unroll") for (int kt = 0; kt < 4; ++kt) { _Pragma("unroll") for (int qt = 0; qt < 2; ++qt) { _Pragma("unroll") for (int i = 0; i < 4; ++i) s[kt][qt][i] = __builtin_amdgcn_exp2f(fmaf(s[kt][qt][i], C, mnC)); } } } while (0)
; template <int LDQ, int LDK, int LDO>
; __device__ __forceinline__ void attn_gqa16_body(const bf16* __restrict__ Qb, const bf16* __restrict__ Kh, const bf16* __restrict__ Vh, bf16* __restrict__ Ob, int seq, char* lds, float mref) {
;     ...
;     SBAR(); pv16<0>(o, vb, pb); SBAR();
;     asm volatile("s_waitcnt vmcnt(0)" ::: "memory");
;     if (t + 2 < NT) HWRITEK(t & 1);
;     if (t + 1 < NT) HWRITEV((t + 1) & 1);
;     HLOADK(t + 3); HLOADV(t + 2);
;     SBAR(); pv16<4>(o, vb, pb); SBAR();
;     if (more) HEXP();
	v_mfma_f32_16x16x32_bf16 v[10:13], v[18:21], v[106:109], v[78:81]
	s_waitcnt lgkmcnt(0)
	v_mfma_f32_16x16x32_bf16 v[18:21], v[18:21], v[110:113], v[50:53]
	v_mfma_f32_16x16x32_bf16 v[10:13], v[22:25], v[114:117], v[10:13]
	v_mfma_f32_16x16x32_bf16 v[22:25], v[22:25], v[118:121], v[18:21]
	v_mfma_f32_16x16x32_bf16 v[18:21], v[14:17], v[106:109], v[82:85]
	v_mfma_f32_16x16x32_bf16 v[50:53], v[14:17], v[110:113], v[86:89]
	v_mfma_f32_16x16x32_bf16 v[14:17], v[30:33], v[114:117], v[18:21]
	v_mfma_f32_16x16x32_bf16 v[18:21], v[30:33], v[118:121], v[50:53]
	s_waitcnt vmcnt(0)
	s_waitcnt vmcnt(1)
	s_waitcnt vmcnt(0)
	ds_read_b64_tr_b16 v[26:27], v183 offset:0x2080
	ds_read_b64_tr_b16 v[28:29], v183 offset:0x2280
	ds_read_b64_tr_b16 v[30:31], v183 offset:0x2480
	ds_read_b64_tr_b16 v[32:33], v183 offset:0x2680
	ds_read_b64_tr_b16 v[34:35], v183 offset:0x28a0
	ds_read_b64_tr_b16 v[36:37], v183 offset:0x2aa0
	ds_read_b64_tr_b16 v[78:79], v183 offset:0x2ca0
	ds_read_b64_tr_b16 v[80:81], v183 offset:0x2ea0
	ds_read_b64_tr_b16 v[82:83], v183 offset:0x30c0
	ds_read_b64_tr_b16 v[84:85], v183 offset:0x32c0
	ds_read_b64_tr_b16 v[86:87], v183 offset:0x34c0
	ds_read_b64_tr_b16 v[88:89], v183 offset:0x36c0
	s_waitcnt lgkmcnt(4)
	s_nop 0
	v_mfma_f32_16x16x32_bf16 v[50:53], v[26:29], v[106:109], v[54:57]
	v_mfma_f32_16x16x32_bf16 v[26:29], v[26:29], v[110:113], v[62:65]
	v_mfma_f32_16x16x32_bf16 v[58:61], v[34:37], v[106:109], v[58:61]
	v_mfma_f32_16x16x32_bf16 v[34:37], v[34:37], v[110:113], v[70:73]
	v_mfma_f32_16x16x32_bf16 v[50:53], v[30:33], v[114:117], v[50:53]
	v_mfma_f32_16x16x32_bf16 v[54:57], v[30:33], v[118:121], v[26:29]
	v_mfma_f32_16x16x32_bf16 v[70:73], v[78:81], v[114:117], v[58:61]
	v_mfma_f32_16x16x32_bf16 v[78:81], v[78:81], v[118:121], v[34:37]
	ds_read_b64_tr_b16 v[30:31], v183 offset:0x38e0
	ds_read_b64_tr_b16 v[32:33], v183 offset:0x3ae0
	ds_read_b64_tr_b16 v[34:35], v183 offset:0x3ce0
	ds_read_b64_tr_b16 v[36:37], v183 offset:0x3ee0
	s_waitcnt lgkmcnt(4)
	v_mfma_f32_16x16x32_bf16 v[26:29], v[82:85], v[106:109], v[42:45]
	s_waitcnt lgkmcnt(0)
	v_mfma_f32_16x16x32_bf16 v[42:45], v[82:85], v[110:113], v[46:49]
	v_mfma_f32_16x16x32_bf16 v[26:29], v[86:89], v[114:117], v[26:29]
	v_mfma_f32_16x16x32_bf16 v[58:61], v[86:89], v[118:121], v[42:45]
	v_mfma_f32_16x16x32_bf16 v[42:45], v[30:33], v[106:109], v[66:69]
	v_mfma_f32_16x16x32_bf16 v[46:49], v[30:33], v[110:113], v[74:77]
	v_mfma_f32_16x16x32_bf16 v[30:33], v[34:37], v[114:117], v[42:45]
	v_mfma_f32_16x16x32_bf16 v[62:65], v[34:37], v[118:121], v[46:49]
	s_nop 4
	v_add_f32_e32 v42, v186, v196
	v_exp_f32_e32 v116, v42
	v_add_f32_e32 v42, v186, v197
	v_exp_f32_e32 v117, v42
	v_add_f32_e32 v42, v186, v198
	v_exp_f32_e32 v118, v42
	v_add_f32_e32 v42, v186, v199
	v_exp_f32_e32 v119, v42
	v_add_f32_e32 v42, v186, v168
	v_add_f32_e32 v34, v186, v146
	v_exp_f32_e32 v98, v42
	v_add_f32_e32 v42, v186, v169
	v_exp_f32_e32 v131, v34
	v_add_f32_e32 v34, v186, v147
	v_exp_f32_e32 v99, v42
	v_add_f32_e32 v42, v186, v170
	v_exp_f32_e32 v133, v34
	v_add_f32_e32 v34, v186, v148
	v_exp_f32_e32 v100, v42
	v_add_f32_e32 v42, v186, v171
	v_exp_f32_e32 v74, v34
	v_add_f32_e32 v34, v186, v149
	v_exp_f32_e32 v101, v42
	v_add_f32_e32 v42, v186, v200
	v_exp_f32_e32 v129, v34
	v_add_f32_e32 v34, v186, v160
	v_exp_f32_e32 v120, v42
	v_add_f32_e32 v42, v186, v201
	v_exp_f32_e32 v123, v34
	v_add_f32_e32 v34, v186, v161
	v_exp_f32_e32 v121, v42
	v_add_f32_e32 v42, v186, v202
	v_exp_f32_e32 v125, v34
	v_add_f32_e32 v34, v186, v162
	v_exp_f32_e32 v75, v42
	v_add_f32_e32 v42, v186, v203
	v_exp_f32_e32 v76, v34
	v_add_f32_e32 v34, v186, v163
	v_exp_f32_e32 v77, v42
	v_add_f32_e32 v42, v186, v134
	v_exp_f32_e32 v87, v34
	v_add_f32_e32 v34, v186, v164
	v_exp_f32_e32 v102, v42
	v_add_f32_e32 v42, v186, v135
	v_exp_f32_e32 v66, v34
	v_add_f32_e32 v34, v186, v165
	v_exp_f32_e32 v103, v42
	v_add_f32_e32 v42, v186, v136
	v_exp_f32_e32 v68, v34
	v_add_f32_e32 v34, v186, v166
	v_exp_f32_e32 v43, v42
	v_exp_f32_e32 v67, v34
	v_add_f32_e32 v34, v186, v167
	v_add_f32_e32 v35, v186, v173
	v_exp_f32_e32 v69, v34
	v_add_f32_e32 v34, v186, v172
	v_exp_f32_e32 v36, v35
	v_add_f32_e32 v35, v186, v174
	v_add_f32_e32 v37, v186, v175
	v_add_f32_e32 v42, v186, v137
	v_exp_f32_e32 v34, v34
	v_exp_f32_e32 v35, v35
	v_exp_f32_e32 v37, v37
	v_exp_f32_e32 v45, v42
	v_add_f32_e32 v42, v143, v151
	v_pk_add_f32 v[48:49], v[144:145], v[144:145] op_sel:[0,1] op_sel_hi:[1,0]
	v_pk_add_f32 v[84:85], v[142:143], v[42:43] op_sel_hi:[1,0]
	v_mov_b32_e32 v49, v76
	v_mov_b32_e32 v85, v87
	v_pk_add_f32 v[46:47], v[122:123], v[124:125]
	v_pk_add_f32 v[48:49], v[48:49], v[84:85]
	v_add_f32_e32 v42, v98, v99
	v_pk_add_f32 v[46:47], v[46:47], v[48:49]
	v_pk_add_f32 v[48:49], v[34:35], v[36:37]
	v_pk_add_f32 v[46:47], v[46:47], v[46:47] op_sel:[0,1] op_sel_hi:[1,0]
	v_pk_add_f32 v[48:49], v[48:49], v[48:49] op_sel:[0,1] op_sel_hi:[1,0]
	v_add_f32_e32 v44, v100, v101
	v_mov_b32_e32 v47, v102
	v_mov_b32_e32 v49, v103
	v_pk_add_f32 v[46:47], v[46:47], v[48:49]
	v_pk_add_f32 v[48:49], v[42:43], v[44:45]
	v_cvt_pk_bf16_f32 v82, v131, v133
	v_cvt_pk_bf16_f32 v83, v74, v129
	v_cvt_pk_bf16_f32 v84, v66, v68
	v_cvt_pk_bf16_f32 v85, v67, v69
	v_cvt_pk_bf16_f32 v86, v123, v125
	s_nop 0
	v_pk_add_f32 v[46:47], v[46:47], v[48:49]
	v_pk_add_f32 v[48:49], v[126:127], v[126:127] op_sel:[0,1] op_sel_hi:[1,0]
	v_add_f32_e32 v122, v46, v47
	v_mov_b32_e32 v49, v74
	v_pk_add_f32 v[46:47], v[130:131], v[132:133]
	v_pk_add_f32 v[48:49], v[48:49], v[128:129]
	v_cvt_pk_bf16_f32 v87, v76, v87
	v_cvt_pk_bf16_f32 v88, v34, v36
	v_cvt_pk_bf16_f32 v89, v35, v37
	v_cvt_pk_bf16_f32 v94, v116, v117
	v_cvt_pk_bf16_f32 v95, v118, v119
	s_nop 0
	v_pk_add_f32 v[114:115], v[46:47], v[48:49]
	v_cvt_pk_bf16_f32 v96, v120, v121
	v_cvt_pk_bf16_f32 v97, v75, v77
	v_cvt_pk_bf16_f32 v98, v98, v99
	v_cvt_pk_bf16_f32 v99, v100, v101
	v_cvt_pk_bf16_f32 v100, v102, v103
	v_cvt_pk_bf16_f32 v101, v43, v45
	s_waitcnt lgkmcnt(0)
	s_barrier
; #define SBAR() __builtin_amdgcn_sched_barrier(0)
; #define MFMA16(a, b, c) __builtin_amdgcn_mfma_f32_16x16x32_bf16(a, b, c, 0, 0, 0)
; template <int D0> __device__ __forceinline__ void pv16(f32x4a (&o)[8][2], int vb, const bf16x8 (&pb)[2][2]) {
;     ...
;   const s16x4 a0 = TR(D0, 0, 0), a1 = TR(D0, 0, 1), a2 = TR(D0, 1, 0), a3 = TR(D0, 1, 1), b0 = TR(D0 + 1, 0, 0), b1 = TR(D0 + 1, 0, 1), b2 = TR(D0 + 1, 1, 0), b3 = TR(D0 + 1, 1, 1);
;   const s16x4 c0 = TR(D0 + 2, 0, 0), c1 = TR(D0 + 2, 0, 1), c2 = TR(D0 + 2, 1, 0), c3 = TR(D0 + 2, 1, 1);
;   asm volatile("s_waitcnt lgkmcnt(4)" ::: "memory"); SBAR();
;   o[D0][0] = MFMA16(PK16(a0, a1), pb[0][0], o[D0][0]); o[D0][1] = MFMA16(PK16(a0, a1), pb[0][1], o[D0][1]);
;   o[D0 + 1][0] = MFMA16(PK16(b0, b1), pb[0][0], o[D0 + 1][0]); o[D0 + 1][1] = MFMA16(PK16(b0, b1), pb[0][1], o[D0 + 1][1]);
;   o[D0][0] = MFMA16(PK16(a2, a3), pb[1][0], o[D0][0]); o[D0][1] = MFMA16(PK16(a2, a3), pb[1][1], o[D0][1]);
;   o[D0 + 1][0] = MFMA16(PK16(b2, b3), pb[1][0], o[D0 + 1][0]); o[D0 + 1][1] = MFMA16(PK16(b2, b3), pb[1][1], o[D0 + 1][1]);
;   SBAR();
;   const s16x4 d0 = TR(D0 + 3, 0, 0), d1 = TR(D0 + 3, 0, 1), d2 = TR(D0 + 3, 1, 0), d3 = TR(D0 + 3, 1, 1);
;   asm volatile("s_waitcnt lgkmcnt(4)" ::: "memory"); SBAR();
;   o[D0 + 2][0] = MFMA16(PK16(c0, c1), pb[0][0], o[D0 + 2][0]); o[D0 + 2][1] = MFMA16(PK16(c0, c1), pb[0][1], o[D0 + 2][1]);
;   o[D0 + 2][0] = MFMA16(PK16(c2, c3), pb[1][0], o[D0 + 2][0]); o[D0 + 2][1] = MFMA16(PK16(c2, c3), pb[1][1], o[D0 + 2][1]);
;   asm volatile("s_waitcnt lgkmcnt(0)" ::: "memory"); SBAR();
;   o[D0 + 3][0] = MFMA16(PK16(d0, d1), pb[0][0], o[D0 + 3][0]); o[D0 + 3][1] = MFMA16(PK16(d0, d1), pb[0][1], o[D0 + 3][1]);
;   o[D0 + 3][0] = MFMA16(PK16(d2, d3), pb[1][0], o[D0 + 3][0]); o[D0 + 3][1] = MFMA16(PK16(d2, d3), pb[1][1], o[D0 + 3][1]);
; template <int LDQ, int LDK, int LDO>
; __device__ __forceinline__ void attn_gqa16_body(const bf16* __restrict__ Qb, const bf16* __restrict__ Kh, const bf16* __restrict__ Vh, bf16* __restrict__ Ob, int seq, char* lds, float mref) {
;     ...
;     SBAR(); pv16<4>(o, vb, pb); SBAR();
;     if (more) HEXP();
;   }
;   __builtin_amdgcn_s_setprio(0);
;   ls0 += __shfl_xor(ls0, 16); ls0 += __shfl_xor(ls0, 32); ls1 += __shfl_xor(ls1, 16); ls1 += __shfl_xor(ls1, 32);
;   const float rl[2] = {__builtin_amdgcn_rcpf(ls0), __builtin_amdgcn_rcpf(ls1)};
	ds_read_b64_tr_b16 v[34:35], v184 offset:0
	ds_read_b64_tr_b16 v[36:37], v184 offset:0x200
	ds_read_b64_tr_b16 v[42:43], v184 offset:0x400
	ds_read_b64_tr_b16 v[44:45], v184 offset:0x600
	ds_read_b64_tr_b16 v[46:47], v184 offset:0x820
	ds_read_b64_tr_b16 v[48:49], v184 offset:0xa20
	ds_read_b64_tr_b16 v[102:103], v184 offset:0xc20
	ds_read_b64_tr_b16 v[104:105], v184 offset:0xe20
	ds_read_b64_tr_b16 v[106:107], v184 offset:0x1040
	ds_read_b64_tr_b16 v[108:109], v184 offset:0x1240
	ds_read_b64_tr_b16 v[110:111], v184 offset:0x1440
	ds_read_b64_tr_b16 v[112:113], v184 offset:0x1640
	s_waitcnt lgkmcnt(4)
	s_nop 0
	v_mfma_f32_16x16x32_bf16 v[2:5], v[34:37], v[82:85], v[2:5]
	v_mfma_f32_16x16x32_bf16 v[6:9], v[34:37], v[86:89], v[6:9]
	v_mfma_f32_16x16x32_bf16 v[34:37], v[46:49], v[82:85], v[38:41]
	v_mfma_f32_16x16x32_bf16 v[46:49], v[46:49], v[86:89], v[90:93]
	v_mfma_f32_16x16x32_bf16 v[38:41], v[42:45], v[94:97], v[2:5]
	v_mfma_f32_16x16x32_bf16 v[6:9], v[42:45], v[98:101], v[6:9]
	v_mfma_f32_16x16x32_bf16 v[34:37], v[102:105], v[94:97], v[34:37]
	v_mfma_f32_16x16x32_bf16 v[2:5], v[102:105], v[98:101], v[46:49]
	ds_read_b64_tr_b16 v[46:47], v184 offset:0x1860
	ds_read_b64_tr_b16 v[48:49], v184 offset:0x1a60
	ds_read_b64_tr_b16 v[90:91], v184 offset:0x1c60
	ds_read_b64_tr_b16 v[92:93], v184 offset:0x1e60
	s_waitcnt lgkmcnt(4)
	v_mfma_f32_16x16x32_bf16 v[10:13], v[106:109], v[82:85], v[10:13]
	s_waitcnt lgkmcnt(0)
	v_mfma_f32_16x16x32_bf16 v[22:25], v[106:109], v[86:89], v[22:25]
	v_mfma_f32_16x16x32_bf16 v[42:45], v[110:113], v[94:97], v[10:13]
	v_mfma_f32_16x16x32_bf16 v[10:13], v[110:113], v[98:101], v[22:25]
	v_mfma_f32_16x16x32_bf16 v[14:17], v[46:49], v[82:85], v[14:17]
	v_mfma_f32_16x16x32_bf16 v[18:21], v[46:49], v[86:89], v[18:21]
	v_mfma_f32_16x16x32_bf16 v[46:49], v[90:93], v[94:97], v[14:17]
	v_mfma_f32_16x16x32_bf16 v[14:17], v[90:93], v[98:101], v[18:21]
	s_waitcnt vmcnt(0)
	ds_read_b64_tr_b16 v[18:19], v184 offset:0x2080
	ds_read_b64_tr_b16 v[20:21], v184 offset:0x2280
	ds_read_b64_tr_b16 v[22:23], v184 offset:0x2480
	ds_read_b64_tr_b16 v[24:25], v184 offset:0x2680
	ds_read_b64_tr_b16 v[90:91], v184 offset:0x28a0
	ds_read_b64_tr_b16 v[92:93], v184 offset:0x2aa0
	ds_read_b64_tr_b16 v[102:103], v184 offset:0x2ca0
	ds_read_b64_tr_b16 v[104:105], v184 offset:0x2ea0
	ds_read_b64_tr_b16 v[106:107], v184 offset:0x30c0
	ds_read_b64_tr_b16 v[108:109], v184 offset:0x32c0
	ds_read_b64_tr_b16 v[110:111], v184 offset:0x34c0
	ds_read_b64_tr_b16 v[112:113], v184 offset:0x36c0
	s_waitcnt lgkmcnt(4)
	s_nop 5
	v_mfma_f32_16x16x32_bf16 v[50:53], v[18:21], v[82:85], v[50:53]
	v_mfma_f32_16x16x32_bf16 v[18:21], v[18:21], v[86:89], v[54:57]
	v_mfma_f32_16x16x32_bf16 v[70:73], v[90:93], v[82:85], v[70:73]
	v_mfma_f32_16x16x32_bf16 v[78:81], v[90:93], v[86:89], v[78:81]
	v_mfma_f32_16x16x32_bf16 v[54:57], v[22:25], v[94:97], v[50:53]
	v_mfma_f32_16x16x32_bf16 v[22:25], v[22:25], v[98:101], v[18:21]
	v_mfma_f32_16x16x32_bf16 v[50:53], v[102:105], v[94:97], v[70:73]
	v_mfma_f32_16x16x32_bf16 v[18:21], v[102:105], v[98:101], v[78:81]
	ds_read_b64_tr_b16 v[70:71], v184 offset:0x38e0
	ds_read_b64_tr_b16 v[72:73], v184 offset:0x3ae0
	ds_read_b64_tr_b16 v[78:79], v184 offset:0x3ce0
	ds_read_b64_tr_b16 v[80:81], v184 offset:0x3ee0
	s_waitcnt lgkmcnt(4)
	v_mfma_f32_16x16x32_bf16 v[26:29], v[106:109], v[82:85], v[26:29]
	s_waitcnt lgkmcnt(0)
	v_mfma_f32_16x16x32_bf16 v[90:93], v[106:109], v[86:89], v[58:61]
	v_mfma_f32_16x16x32_bf16 v[58:61], v[110:113], v[94:97], v[26:29]
	v_mfma_f32_16x16x32_bf16 v[26:29], v[110:113], v[98:101], v[90:93]
	v_mfma_f32_16x16x32_bf16 v[30:33], v[70:73], v[82:85], v[30:33]
	v_mfma_f32_16x16x32_bf16 v[70:73], v[70:73], v[86:89], v[62:65]
	v_mfma_f32_16x16x32_bf16 v[62:65], v[78:81], v[94:97], v[30:33]
	v_mfma_f32_16x16x32_bf16 v[30:33], v[78:81], v[98:101], v[70:73]
	v_add_f32_e64 v66, v66, v68
	v_add_f32_e64 v67, v67, v69
	v_pk_add_f32 v[68:69], v[114:115], v[114:115] op_sel:[0,1] op_sel_hi:[1,0]
	v_pk_add_f32 v[66:67], v[66:67], v[66:67] op_sel:[0,1] op_sel_hi:[1,0]
	v_add_f32_e32 v74, v116, v117
	v_add_f32_e32 v76, v118, v119
	v_mov_b32_e32 v69, v120
	v_mov_b32_e32 v67, v121
	v_pk_add_f32 v[66:67], v[68:69], v[66:67]
	v_pk_add_f32 v[68:69], v[74:75], v[76:77]
	s_nop 0
	v_pk_add_f32 v[66:67], v[66:67], v[68:69]
	s_nop 0
	v_add_f32_e32 v66, v66, v67
	s_setprio 0
	ds_bpermute_b32 v67, v177, v66
	ds_bpermute_b32 v68, v177, v122
	v_mov_b32_e32 v70, v185
	s_waitcnt lgkmcnt(1)
	v_add_f32_e32 v66, v66, v67
	s_waitcnt lgkmcnt(0)
	v_add_f32_e32 v67, v122, v68
	ds_bpermute_b32 v68, v188, v66
	ds_bpermute_b32 v69, v188, v67
	s_waitcnt lgkmcnt(1)
	v_add_f32_e32 v66, v66, v68
	s_waitcnt lgkmcnt(0)
	v_add_f32_e32 v67, v67, v69
	v_rcp_f32_e32 v68, v66
	v_rcp_f32_e32 v66, v67
	v_mov_b32_e32 v67, v176
	v_mov_b32_e32 v69, v180
	s_branch .LBB0_641
